# L: phase-E ctx o-proj units publish with write-through (sc1) stores + vmcnt(0) instead of plain stores + L2 writeback before the batch counter
# baseline (speedup 1.0000x reference)
;     __device__ __forceinline__ void operator()(const pg8::f32x4 (&acc)[2][2][4][2], const pg8::Unit& u, int wr, int wc, int fr, int fq) const {
;         const int col0 = u.pn * 256 + wc * 32 + 8 * fq;
;         const int cr = (u.pm % 9) == 0 ? 8 : u.pm / 9;
;         f32x4 bv[2][2], gv[2][2];
; #pragma unroll
;         for (int bj = 0; bj < 2; ++bj)
; #pragma unroll
;             for (int n = 0; n < 2; ++n) { const int c = col0 + bj * 128 + 4 * n;
;                 bv[bj][n] = bias ? *(const f32x4*)(bias + c) : (f32x4){0.f, 0.f, 0.f, 0.f}; gv[bj][n] = *(const f32x4*)(gate + (size_t)cr * 6144 + c); }
; #pragma unroll
;         for (int ai = 0; ai < 2; ++ai) if (ai < nai)
; #pragma unroll
;             for (int m = 0; m < 4; ++m) { const size_t row = (size_t)(u.pm * 256 + rowoff + ai * 128 + wr * 64 + m * 16 + fr); bf16_t* rowp = X + row * 1024 + col0; float sq = 0.f;
; #pragma unroll
;                 for (int bj = 0; bj < 2; ++bj) { pg8::u32x4* ptr = (pg8::u32x4*)(rowp + bj * 128); const pg8::u32x4 xo = *ptr;
;                     const f32x4 v0 = gv[bj][0] * (acc[ai][bj][m][0] + bv[bj][0]), v1 = gv[bj][1] * (acc[ai][bj][m][1] + bv[bj][1]);
;                     pg8::u32x4 w;
;                     w.x = pg8::cvt_pk_bf16(bf2f(xo.x & 0xffffu) + v0[0], bf2f(xo.x >> 16) + v0[1]); w.y = pg8::cvt_pk_bf16(bf2f(xo.y & 0xffffu) + v0[2], bf2f(xo.y >> 16) + v0[3]);
;                     w.z = pg8::cvt_pk_bf16(bf2f(xo.z & 0xffffu) + v1[0], bf2f(xo.z >> 16) + v1[1]); w.w = pg8::cvt_pk_bf16(bf2f(xo.w & 0xffffu) + v1[2], bf2f(xo.w >> 16) + v1[3]);
;                     *ptr = w;
;                     { const float r0 = bf2f(w.x & 0xffffu), r1 = bf2f(w.x >> 16), r2 = bf2f(w.y & 0xffffu), r3 = bf2f(w.y >> 16), r4 = bf2f(w.z & 0xffffu), r5 = bf2f(w.z >> 16), r6 = bf2f(w.w & 0xffffu), r7 = bf2f(w.w >> 16);
;                       sq += (r0 * r0 + r1 * r1) + (r2 * r2 + r3 * r3) + (r4 * r4 + r5 * r5) + (r6 * r6 + r7 * r7); } }
;                 sq += __shfl_xor(sq, 16); sq += __shfl_xor(sq, 32);
;                 if (fq == 0) ssq[row * 16 + u.pn * 4 + wc] = sq; }
; __device__ __forceinline__ void phaseE(const Params& p, int layer, LAS unsigned char* lds, int bid, int nb) {
;     ...
;     if (special) {
;         oproj_ctx_unit(p, layer, lds, bid >> 3, bid & 3, (bid >> 2) & 1);
;         unsigned* ctr = (unsigned*)(p.ws + ws::CTL) + CW_CTXC + (layer * 8 + (bid >> 3)) * 64;
.LBB0_1273:
	v_readlane_b32 s0, v253, 60
	v_lshlrev_b32_e32 v2, 1, v100
	v_mov_b32_e32 v101, 0x210
	v_add_u32_e32 v98, s0, v1
	v_ashrrev_i32_e32 v99, 31, v98
	v_readlane_b32 s0, v250, 6
	v_lshlrev_b64 v[102:103], 11, v[98:99]
	v_readlane_b32 s1, v250, 7
	v_lshl_or_b32 v110, v100, 2, v101
	s_waitcnt vmcnt(0)
	v_pk_add_f32 v[94:95], v[94:95], v[34:35]
	v_lshl_add_u64 v[102:103], s[0:1], 0, v[102:103]
	v_lshl_add_u64 v[106:107], v[102:103], 0, v[2:3]
	global_load_dwordx4 v[102:105], v[106:107], off
	v_pk_add_f32 v[92:93], v[92:93], v[32:33]
	v_pk_add_f32 v[66:67], v[66:67], v[30:31]
	v_pk_add_f32 v[100:101], v[64:65], v[28:29]
	v_pk_mul_f32 v[94:95], v[46:47], v[94:95]
	v_pk_mul_f32 v[92:93], v[44:45], v[92:93]
	v_pk_mul_f32 v[108:109], v[54:55], v[66:67]
	global_load_dwordx4 v[64:67], v110, s[4:5]
	v_pk_mul_f32 v[100:101], v[52:53], v[100:101]
	v_pk_add_f32 v[88:89], v[88:89], v[40:41]
	v_pk_add_f32 v[90:91], v[90:91], v[42:43]
	v_pk_add_f32 v[86:87], v[86:87], v[38:39]
	v_pk_add_f32 v[84:85], v[84:85], v[36:37]
	v_pk_mul_f32 v[90:91], v[50:51], v[90:91]
	s_waitcnt vmcnt(0)
	v_lshlrev_b32_e32 v110, 16, v102
	v_and_b32_e32 v102, 0xffff0000, v102
	v_lshlrev_b32_e32 v111, 16, v103
	v_and_b32_e32 v103, 0xffff0000, v103
	v_lshlrev_b32_e32 v112, 16, v104
	v_and_b32_e32 v104, 0xffff0000, v104
	v_lshlrev_b32_e32 v113, 16, v105
	v_and_b32_e32 v105, 0xffff0000, v105
	v_add_f32_e32 v92, v92, v110
	v_add_f32_e32 v93, v93, v102
	v_add_f32_e32 v94, v94, v111
	v_add_f32_e32 v95, v95, v103
	v_add_f32_e32 v100, v100, v112
	v_add_f32_e32 v101, v101, v104
	v_add_f32_e32 v102, v108, v113
	v_add_f32_e32 v103, v109, v105
	v_cvt_pk_bf16_f32 v92, v92, v93
	v_cvt_pk_bf16_f32 v93, v94, v95
	v_cvt_pk_bf16_f32 v94, v100, v101
	v_cvt_pk_bf16_f32 v95, v102, v103
	global_load_dwordx4 v[100:103], v[106:107], off offset:256
	v_and_b32_e32 v109, 64, v207
	v_xor_b32_e32 v108, 16, v207
	v_pk_mul_f32 v[104:105], v[48:49], v[88:89]
	v_add_u32_e32 v89, 64, v109
	v_cmp_lt_i32_e32 vcc, v108, v89
	global_store_dwordx4 v[106:107], v[92:95], off sc1
	v_lshlrev_b32_e32 v109, 16, v93
	v_cndmask_b32_e32 v88, v207, v108, vcc
	v_lshlrev_b32_e32 v108, 16, v92
	v_and_b32_e32 v92, 0xffff0000, v92
	v_and_b32_e32 v93, 0xffff0000, v93
	v_lshlrev_b32_e32 v110, 16, v94
	v_and_b32_e32 v94, 0xffff0000, v94
	v_mul_f32_e32 v92, v92, v92
	v_mul_f32_e32 v93, v93, v93
	v_lshlrev_b32_e32 v111, 16, v95
	v_and_b32_e32 v95, 0xffff0000, v95
	v_mul_f32_e32 v94, v94, v94
	v_fmac_f32_e32 v92, v108, v108
	v_fmac_f32_e32 v93, v109, v109
	v_mul_f32_e32 v95, v95, v95
	v_fmac_f32_e32 v94, v110, v110
	v_add_f32_e32 v92, v92, v93
	v_fmac_f32_e32 v95, v111, v111
	v_add_f32_e32 v92, v92, v94
	v_pk_mul_f32 v[86:87], v[66:67], v[86:87]
	v_pk_mul_f32 v[84:85], v[64:65], v[84:85]
	v_add_f32_e32 v94, v92, v95
	v_lshlrev_b32_e32 v88, 2, v88
	s_waitcnt vmcnt(0)
	v_lshlrev_b32_e32 v92, 16, v100
	v_and_b32_e32 v93, 0xffff0000, v100
	v_lshlrev_b32_e32 v95, 16, v101
	v_and_b32_e32 v100, 0xffff0000, v101
	v_lshlrev_b32_e32 v101, 16, v102
	v_and_b32_e32 v102, 0xffff0000, v102
	v_lshlrev_b32_e32 v108, 16, v103
	v_and_b32_e32 v103, 0xffff0000, v103
	v_add_f32_e32 v92, v104, v92
	v_add_f32_e32 v93, v105, v93
	v_add_f32_e32 v91, v91, v100
	v_add_f32_e32 v85, v85, v102
	v_add_f32_e32 v87, v87, v103
	v_add_f32_e32 v95, v90, v95
	v_add_f32_e32 v84, v84, v101
	v_add_f32_e32 v86, v86, v108
	v_cvt_pk_bf16_f32 v90, v92, v93
	v_cvt_pk_bf16_f32 v91, v95, v91
	v_cvt_pk_bf16_f32 v92, v84, v85
	v_cvt_pk_bf16_f32 v93, v86, v87
	global_store_dwordx4 v[106:107], v[90:93], off offset:256 sc1
	v_and_b32_e32 v85, 0xffff0000, v90
	v_and_b32_e32 v87, 0xffff0000, v91
	v_lshlrev_b32_e32 v84, 16, v90
	v_lshlrev_b32_e32 v86, 16, v91
	v_and_b32_e32 v100, 0xffff0000, v92
	v_mul_f32_e32 v85, v85, v85
	v_mul_f32_e32 v87, v87, v87
	v_lshlrev_b32_e32 v95, 16, v92
	v_and_b32_e32 v102, 0xffff0000, v93
	v_mul_f32_e32 v100, v100, v100
	v_fmac_f32_e32 v85, v84, v84
	v_fmac_f32_e32 v87, v86, v86
	v_lshlrev_b32_e32 v101, 16, v93
	v_mul_f32_e32 v102, v102, v102
	v_fmac_f32_e32 v100, v95, v95
	v_add_f32_e32 v84, v85, v87
	v_fmac_f32_e32 v102, v101, v101
	v_add_f32_e32 v84, v84, v100
	v_add_f32_e32 v84, v84, v102
	v_add_f32_e32 v84, v94, v84
	ds_bpermute_b32 v85, v88, v84
	v_xor_b32_e32 v86, 32, v207
	v_cmp_lt_i32_e32 vcc, v86, v89
	s_waitcnt lgkmcnt(0)
	v_add_f32_e32 v84, v84, v85
	v_cndmask_b32_e32 v86, v207, v86, vcc
	v_lshlrev_b32_e32 v89, 2, v86
	ds_bpermute_b32 v85, v89, v84
	v_cmp_eq_u32_e32 vcc, 0, v97
	s_and_saveexec_b64 s[0:1], vcc
	s_cbranch_execz .LBB0_1275
	v_readlane_b32 s4, v253, 56
	s_waitcnt lgkmcnt(0)
	v_add_f32_e32 v86, v84, v85
	v_lshlrev_b64 v[84:85], 6, v[98:99]
	v_readlane_b32 s5, v253, 57
	s_lshl_b32 s30, s12, 2
	s_nop 0
	v_lshl_add_u64 v[84:85], s[4:5], 0, v[84:85]
	v_lshl_add_u64 v[84:85], v[84:85], 0, s[30:31]
	global_store_dword v[84:85], v86, off sc1
; __device__ __forceinline__ unsigned cvt_pk_bf16(float lo, float hi) { unsigned r; asm volatile("v_cvt_pk_bf16_f32 %0, %1, %2" : "=v"(r) : "v"(lo), "v"(hi)); return r; }
;     __device__ __forceinline__ void operator()(const pg8::f32x4 (&acc)[2][2][4][2], const pg8::Unit& u, int wr, int wc, int fr, int fq) const {
;     ...
;             for (int m = 0; m < 4; ++m) { const size_t row = (size_t)(u.pm * 256 + rowoff + ai * 128 + wr * 64 + m * 16 + fr); bf16_t* rowp = X + row * 1024 + col0; float sq = 0.f;
; #pragma unroll
;                 for (int bj = 0; bj < 2; ++bj) { pg8::u32x4* ptr = (pg8::u32x4*)(rowp + bj * 128); const pg8::u32x4 xo = *ptr;
;                     const f32x4 v0 = gv[bj][0] * (acc[ai][bj][m][0] + bv[bj][0]), v1 = gv[bj][1] * (acc[ai][bj][m][1] + bv[bj][1]);
;                     pg8::u32x4 w;
;                     w.x = pg8::cvt_pk_bf16(bf2f(xo.x & 0xffffu) + v0[0], bf2f(xo.x >> 16) + v0[1]); w.y = pg8::cvt_pk_bf16(bf2f(xo.y & 0xffffu) + v0[2], bf2f(xo.y >> 16) + v0[3]);
;                     w.z = pg8::cvt_pk_bf16(bf2f(xo.z & 0xffffu) + v1[0], bf2f(xo.z >> 16) + v1[1]); w.w = pg8::cvt_pk_bf16(bf2f(xo.w & 0xffffu) + v1[2], bf2f(xo.w >> 16) + v1[3]);
;                     *ptr = w;
;                     { const float r0 = bf2f(w.x & 0xffffu), r1 = bf2f(w.x >> 16), r2 = bf2f(w.y & 0xffffu), r3 = bf2f(w.y >> 16), r4 = bf2f(w.z & 0xffffu), r5 = bf2f(w.z >> 16), r6 = bf2f(w.w & 0xffffu), r7 = bf2f(w.w >> 16);
;                       sq += (r0 * r0 + r1 * r1) + (r2 * r2 + r3 * r3) + (r4 * r4 + r5 * r5) + (r6 * r6 + r7 * r7); } }
;                 sq += __shfl_xor(sq, 16); sq += __shfl_xor(sq, 32);
;                 if (fq == 0) ssq[row * 16 + u.pn * 4 + wc] = sq; }
.LBB0_1275:
	s_or_b64 exec, exec, s[0:1]
	v_readlane_b32 s0, v253, 58
	v_pk_add_f32 v[80:81], v[80:81], v[32:33]
	v_pk_add_f32 v[78:79], v[78:79], v[30:31]
	v_add_u32_e32 v84, s0, v1
	s_waitcnt lgkmcnt(0)
	v_ashrrev_i32_e32 v85, 31, v84
	v_readlane_b32 s0, v250, 6
	v_lshlrev_b64 v[86:87], 11, v[84:85]
	v_readlane_b32 s1, v250, 7
	v_pk_add_f32 v[76:77], v[76:77], v[28:29]
	v_pk_mul_f32 v[80:81], v[44:45], v[80:81]
	v_lshl_add_u64 v[86:87], s[0:1], 0, v[86:87]
	v_lshl_add_u64 v[86:87], v[86:87], 0, v[2:3]
	global_load_dwordx4 v[90:93], v[86:87], off
	v_pk_mul_f32 v[94:95], v[54:55], v[78:79]
	v_pk_mul_f32 v[78:79], v[52:53], v[76:77]
	v_pk_add_f32 v[82:83], v[82:83], v[34:35]
	v_pk_add_f32 v[72:73], v[72:73], v[40:41]
	v_pk_mul_f32 v[82:83], v[46:47], v[82:83]
	v_pk_add_f32 v[70:71], v[70:71], v[38:39]
	v_pk_add_f32 v[68:69], v[68:69], v[36:37]
	v_pk_mul_f32 v[72:73], v[48:49], v[72:73]
	v_pk_add_f32 v[74:75], v[74:75], v[42:43]
	s_waitcnt vmcnt(0)
	v_lshlrev_b32_e32 v76, 16, v90
	v_and_b32_e32 v77, 0xffff0000, v90
	v_add_f32_e32 v76, v80, v76
	v_add_f32_e32 v77, v81, v77
	v_cvt_pk_bf16_f32 v76, v76, v77
	v_lshlrev_b32_e32 v77, 16, v91
	v_and_b32_e32 v80, 0xffff0000, v91
	v_add_f32_e32 v77, v82, v77
	v_add_f32_e32 v80, v83, v80
	v_cvt_pk_bf16_f32 v77, v77, v80
	v_lshlrev_b32_e32 v80, 16, v92
	v_add_f32_e32 v78, v78, v80
	v_and_b32_e32 v80, 0xffff0000, v92
	v_add_f32_e32 v79, v79, v80
	v_cvt_pk_bf16_f32 v78, v78, v79
	v_lshlrev_b32_e32 v79, 16, v93
	v_and_b32_e32 v80, 0xffff0000, v93
	v_add_f32_e32 v79, v94, v79
	v_add_f32_e32 v80, v95, v80
	v_cvt_pk_bf16_f32 v79, v79, v80
	global_store_dwordx4 v[86:87], v[76:79], off sc1
	v_lshlrev_b32_e32 v80, 16, v76
	v_lshlrev_b32_e32 v81, 16, v77
	v_and_b32_e32 v76, 0xffff0000, v76
	v_and_b32_e32 v77, 0xffff0000, v77
	v_mul_f32_e32 v76, v76, v76
	v_mul_f32_e32 v77, v77, v77
	v_lshlrev_b32_e32 v82, 16, v78
	v_and_b32_e32 v78, 0xffff0000, v78
	v_fmac_f32_e32 v76, v80, v80
	v_fmac_f32_e32 v77, v81, v81
	v_add_f32_e32 v76, v76, v77
	v_mul_f32_e32 v77, v78, v78
	v_lshlrev_b32_e32 v83, 16, v79
	v_and_b32_e32 v79, 0xffff0000, v79
	v_fmac_f32_e32 v77, v82, v82
	v_add_f32_e32 v76, v76, v77
	v_mul_f32_e32 v77, v79, v79
	v_fmac_f32_e32 v77, v83, v83
	v_add_f32_e32 v82, v76, v77
	global_load_dwordx4 v[76:79], v[86:87], off offset:256
	v_pk_mul_f32 v[80:81], v[66:67], v[70:71]
	v_pk_mul_f32 v[70:71], v[64:65], v[68:69]
	v_pk_mul_f32 v[74:75], v[50:51], v[74:75]
	s_waitcnt vmcnt(0)
	v_lshlrev_b32_e32 v68, 16, v76
	v_and_b32_e32 v69, 0xffff0000, v76
	v_add_f32_e32 v68, v72, v68
	v_add_f32_e32 v69, v73, v69
	v_cvt_pk_bf16_f32 v68, v68, v69
	v_lshlrev_b32_e32 v69, 16, v77
	v_and_b32_e32 v72, 0xffff0000, v77
	v_add_f32_e32 v69, v74, v69
	v_add_f32_e32 v72, v75, v72
	v_cvt_pk_bf16_f32 v69, v69, v72
	v_lshlrev_b32_e32 v72, 16, v78
	v_add_f32_e32 v70, v70, v72
	v_and_b32_e32 v72, 0xffff0000, v78
	v_add_f32_e32 v71, v71, v72
	v_cvt_pk_bf16_f32 v70, v70, v71
	v_lshlrev_b32_e32 v71, 16, v79
	v_and_b32_e32 v72, 0xffff0000, v79
	v_add_f32_e32 v71, v80, v71
	v_add_f32_e32 v72, v81, v72
	v_cvt_pk_bf16_f32 v71, v71, v72
	global_store_dwordx4 v[86:87], v[68:71], off offset:256 sc1
	v_lshlrev_b32_e32 v72, 16, v68
	v_lshlrev_b32_e32 v73, 16, v69
	v_and_b32_e32 v68, 0xffff0000, v68
	v_and_b32_e32 v69, 0xffff0000, v69
	v_mul_f32_e32 v68, v68, v68
	v_mul_f32_e32 v69, v69, v69
	v_lshlrev_b32_e32 v74, 16, v70
	v_and_b32_e32 v70, 0xffff0000, v70
	v_fmac_f32_e32 v68, v72, v72
	v_fmac_f32_e32 v69, v73, v73
	v_add_f32_e32 v68, v68, v69
	v_mul_f32_e32 v69, v70, v70
	v_lshlrev_b32_e32 v75, 16, v71
	v_and_b32_e32 v71, 0xffff0000, v71
	v_fmac_f32_e32 v69, v74, v74
	v_add_f32_e32 v68, v68, v69
	v_mul_f32_e32 v69, v71, v71
	v_fmac_f32_e32 v69, v75, v75
	v_add_f32_e32 v68, v68, v69
	v_add_f32_e32 v68, v82, v68
	ds_bpermute_b32 v69, v88, v68
	s_waitcnt lgkmcnt(0)
	v_add_f32_e32 v68, v68, v69
	ds_bpermute_b32 v69, v89, v68
	s_and_saveexec_b64 s[0:1], vcc
	s_cbranch_execz .LBB0_1277
	v_readlane_b32 s4, v253, 56
	s_waitcnt lgkmcnt(0)
	v_add_f32_e32 v70, v68, v69
	v_lshlrev_b64 v[68:69], 6, v[84:85]
	v_readlane_b32 s5, v253, 57
	s_lshl_b32 s30, s12, 2
	s_nop 0
	v_lshl_add_u64 v[68:69], s[4:5], 0, v[68:69]
	v_lshl_add_u64 v[68:69], v[68:69], 0, s[30:31]
	global_store_dword v[68:69], v70, off sc1
; __device__ __forceinline__ unsigned cvt_pk_bf16(float lo, float hi) { unsigned r; asm volatile("v_cvt_pk_bf16_f32 %0, %1, %2" : "=v"(r) : "v"(lo), "v"(hi)); return r; }
;     __device__ __forceinline__ void operator()(const pg8::f32x4 (&acc)[2][2][4][2], const pg8::Unit& u, int wr, int wc, int fr, int fq) const {
;     ...
;             for (int m = 0; m < 4; ++m) { const size_t row = (size_t)(u.pm * 256 + rowoff + ai * 128 + wr * 64 + m * 16 + fr); bf16_t* rowp = X + row * 1024 + col0; float sq = 0.f;
; #pragma unroll
;                 for (int bj = 0; bj < 2; ++bj) { pg8::u32x4* ptr = (pg8::u32x4*)(rowp + bj * 128); const pg8::u32x4 xo = *ptr;
;                     const f32x4 v0 = gv[bj][0] * (acc[ai][bj][m][0] + bv[bj][0]), v1 = gv[bj][1] * (acc[ai][bj][m][1] + bv[bj][1]);
;                     pg8::u32x4 w;
;                     w.x = pg8::cvt_pk_bf16(bf2f(xo.x & 0xffffu) + v0[0], bf2f(xo.x >> 16) + v0[1]); w.y = pg8::cvt_pk_bf16(bf2f(xo.y & 0xffffu) + v0[2], bf2f(xo.y >> 16) + v0[3]);
;                     w.z = pg8::cvt_pk_bf16(bf2f(xo.z & 0xffffu) + v1[0], bf2f(xo.z >> 16) + v1[1]); w.w = pg8::cvt_pk_bf16(bf2f(xo.w & 0xffffu) + v1[2], bf2f(xo.w >> 16) + v1[3]);
;                     *ptr = w;
;                     { const float r0 = bf2f(w.x & 0xffffu), r1 = bf2f(w.x >> 16), r2 = bf2f(w.y & 0xffffu), r3 = bf2f(w.y >> 16), r4 = bf2f(w.z & 0xffffu), r5 = bf2f(w.z >> 16), r6 = bf2f(w.w & 0xffffu), r7 = bf2f(w.w >> 16);
;                       sq += (r0 * r0 + r1 * r1) + (r2 * r2 + r3 * r3) + (r4 * r4 + r5 * r5) + (r6 * r6 + r7 * r7); } }
;                 sq += __shfl_xor(sq, 16); sq += __shfl_xor(sq, 32);
;                 if (fq == 0) ssq[row * 16 + u.pn * 4 + wc] = sq; }
.LBB0_1277:
	s_or_b64 exec, exec, s[0:1]
	v_readlane_b32 s0, v253, 59
	v_pk_add_f32 v[60:61], v[60:61], v[32:33]
	v_pk_add_f32 v[58:59], v[58:59], v[30:31]
	v_add_u32_e32 v68, s0, v1
	s_waitcnt lgkmcnt(0)
	v_ashrrev_i32_e32 v69, 31, v68
	v_readlane_b32 s0, v250, 6
	v_lshlrev_b64 v[70:71], 11, v[68:69]
	v_readlane_b32 s1, v250, 7
	v_pk_add_f32 v[56:57], v[56:57], v[28:29]
	v_pk_mul_f32 v[60:61], v[44:45], v[60:61]
	v_lshl_add_u64 v[70:71], s[0:1], 0, v[70:71]
	v_lshl_add_u64 v[70:71], v[70:71], 0, v[2:3]
	global_load_dwordx4 v[72:75], v[70:71], off
	v_pk_mul_f32 v[76:77], v[54:55], v[58:59]
	v_pk_mul_f32 v[58:59], v[52:53], v[56:57]
	v_pk_add_f32 v[62:63], v[62:63], v[34:35]
	v_pk_add_f32 v[24:25], v[24:25], v[40:41]
	v_pk_mul_f32 v[62:63], v[46:47], v[62:63]
	v_pk_add_f32 v[22:23], v[22:23], v[38:39]
	v_pk_add_f32 v[20:21], v[20:21], v[36:37]
	v_pk_mul_f32 v[24:25], v[48:49], v[24:25]
	v_pk_add_f32 v[26:27], v[26:27], v[42:43]
	s_waitcnt vmcnt(0)
	v_lshlrev_b32_e32 v56, 16, v72
	v_and_b32_e32 v57, 0xffff0000, v72
	v_add_f32_e32 v56, v60, v56
	v_add_f32_e32 v57, v61, v57
	v_cvt_pk_bf16_f32 v56, v56, v57
	v_lshlrev_b32_e32 v57, 16, v73
	v_and_b32_e32 v60, 0xffff0000, v73
	v_add_f32_e32 v57, v62, v57
	v_add_f32_e32 v60, v63, v60
	v_cvt_pk_bf16_f32 v57, v57, v60
	v_lshlrev_b32_e32 v60, 16, v74
	v_add_f32_e32 v58, v58, v60
	v_and_b32_e32 v60, 0xffff0000, v74
	v_add_f32_e32 v59, v59, v60
	v_cvt_pk_bf16_f32 v58, v58, v59
	v_lshlrev_b32_e32 v59, 16, v75
	v_and_b32_e32 v60, 0xffff0000, v75
	v_add_f32_e32 v59, v76, v59
	v_add_f32_e32 v60, v77, v60
	v_cvt_pk_bf16_f32 v59, v59, v60
	global_store_dwordx4 v[70:71], v[56:59], off sc1
	v_lshlrev_b32_e32 v60, 16, v56
	v_lshlrev_b32_e32 v61, 16, v57
	v_and_b32_e32 v56, 0xffff0000, v56
	v_and_b32_e32 v57, 0xffff0000, v57
	v_mul_f32_e32 v56, v56, v56
	v_mul_f32_e32 v57, v57, v57
	v_lshlrev_b32_e32 v62, 16, v58
	v_and_b32_e32 v58, 0xffff0000, v58
	v_fmac_f32_e32 v56, v60, v60
	v_fmac_f32_e32 v57, v61, v61
	v_add_f32_e32 v56, v56, v57
	v_mul_f32_e32 v57, v58, v58
	v_lshlrev_b32_e32 v63, 16, v59
	v_and_b32_e32 v59, 0xffff0000, v59
	v_fmac_f32_e32 v57, v62, v62
	v_add_f32_e32 v56, v56, v57
	v_mul_f32_e32 v57, v59, v59
	v_fmac_f32_e32 v57, v63, v63
	v_add_f32_e32 v62, v56, v57
	global_load_dwordx4 v[56:59], v[70:71], off offset:256
	v_pk_mul_f32 v[60:61], v[66:67], v[22:23]
	v_pk_mul_f32 v[22:23], v[64:65], v[20:21]
	v_pk_mul_f32 v[26:27], v[50:51], v[26:27]
	s_waitcnt vmcnt(0)
	v_lshlrev_b32_e32 v20, 16, v56
	v_and_b32_e32 v21, 0xffff0000, v56
	v_add_f32_e32 v20, v24, v20
	v_add_f32_e32 v21, v25, v21
	v_cvt_pk_bf16_f32 v20, v20, v21
	v_lshlrev_b32_e32 v21, 16, v57
	v_and_b32_e32 v24, 0xffff0000, v57
	v_add_f32_e32 v21, v26, v21
	v_add_f32_e32 v24, v27, v24
	v_cvt_pk_bf16_f32 v21, v21, v24
	v_lshlrev_b32_e32 v24, 16, v58
	v_add_f32_e32 v22, v22, v24
	v_and_b32_e32 v24, 0xffff0000, v58
	v_add_f32_e32 v23, v23, v24
	v_cvt_pk_bf16_f32 v22, v22, v23
	v_lshlrev_b32_e32 v23, 16, v59
	v_and_b32_e32 v24, 0xffff0000, v59
	v_add_f32_e32 v23, v60, v23
	v_add_f32_e32 v24, v61, v24
	v_cvt_pk_bf16_f32 v23, v23, v24
	global_store_dwordx4 v[70:71], v[20:23], off offset:256 sc1
	v_lshlrev_b32_e32 v24, 16, v20
	v_lshlrev_b32_e32 v25, 16, v21
	v_and_b32_e32 v20, 0xffff0000, v20
	v_and_b32_e32 v21, 0xffff0000, v21
	v_mul_f32_e32 v20, v20, v20
	v_mul_f32_e32 v21, v21, v21
	v_lshlrev_b32_e32 v26, 16, v22
	v_and_b32_e32 v22, 0xffff0000, v22
	v_fmac_f32_e32 v20, v24, v24
	v_fmac_f32_e32 v21, v25, v25
	v_add_f32_e32 v20, v20, v21
	v_mul_f32_e32 v21, v22, v22
	v_lshlrev_b32_e32 v27, 16, v23
	v_and_b32_e32 v23, 0xffff0000, v23
	v_fmac_f32_e32 v21, v26, v26
	v_add_f32_e32 v20, v20, v21
	v_mul_f32_e32 v21, v23, v23
	v_fmac_f32_e32 v21, v27, v27
	v_add_f32_e32 v20, v20, v21
	v_add_f32_e32 v20, v62, v20
	ds_bpermute_b32 v21, v88, v20
	s_waitcnt lgkmcnt(0)
	v_add_f32_e32 v20, v20, v21
	ds_bpermute_b32 v21, v89, v20
	s_and_saveexec_b64 s[0:1], vcc
	s_cbranch_execz .LBB0_1279
	v_readlane_b32 s4, v253, 56
	s_waitcnt lgkmcnt(0)
	v_add_f32_e32 v22, v20, v21
	v_lshlrev_b64 v[20:21], 6, v[68:69]
	v_readlane_b32 s5, v253, 57
	s_lshl_b32 s30, s12, 2
	s_nop 0
	v_lshl_add_u64 v[20:21], s[4:5], 0, v[20:21]
	v_lshl_add_u64 v[20:21], v[20:21], 0, s[30:31]
	global_store_dword v[20:21], v22, off sc1
; __device__ __forceinline__ unsigned cvt_pk_bf16(float lo, float hi) { unsigned r; asm volatile("v_cvt_pk_bf16_f32 %0, %1, %2" : "=v"(r) : "v"(lo), "v"(hi)); return r; }
;     __device__ __forceinline__ void operator()(const pg8::f32x4 (&acc)[2][2][4][2], const pg8::Unit& u, int wr, int wc, int fr, int fq) const {
;     ...
;             for (int m = 0; m < 4; ++m) { const size_t row = (size_t)(u.pm * 256 + rowoff + ai * 128 + wr * 64 + m * 16 + fr); bf16_t* rowp = X + row * 1024 + col0; float sq = 0.f;
; #pragma unroll
;                 for (int bj = 0; bj < 2; ++bj) { pg8::u32x4* ptr = (pg8::u32x4*)(rowp + bj * 128); const pg8::u32x4 xo = *ptr;
;                     const f32x4 v0 = gv[bj][0] * (acc[ai][bj][m][0] + bv[bj][0]), v1 = gv[bj][1] * (acc[ai][bj][m][1] + bv[bj][1]);
;                     pg8::u32x4 w;
;                     w.x = pg8::cvt_pk_bf16(bf2f(xo.x & 0xffffu) + v0[0], bf2f(xo.x >> 16) + v0[1]); w.y = pg8::cvt_pk_bf16(bf2f(xo.y & 0xffffu) + v0[2], bf2f(xo.y >> 16) + v0[3]);
;                     w.z = pg8::cvt_pk_bf16(bf2f(xo.z & 0xffffu) + v1[0], bf2f(xo.z >> 16) + v1[1]); w.w = pg8::cvt_pk_bf16(bf2f(xo.w & 0xffffu) + v1[2], bf2f(xo.w >> 16) + v1[3]);
;                     *ptr = w;
;                     { const float r0 = bf2f(w.x & 0xffffu), r1 = bf2f(w.x >> 16), r2 = bf2f(w.y & 0xffffu), r3 = bf2f(w.y >> 16), r4 = bf2f(w.z & 0xffffu), r5 = bf2f(w.z >> 16), r6 = bf2f(w.w & 0xffffu), r7 = bf2f(w.w >> 16);
;                       sq += (r0 * r0 + r1 * r1) + (r2 * r2 + r3 * r3) + (r4 * r4 + r5 * r5) + (r6 * r6 + r7 * r7); } }
;                 sq += __shfl_xor(sq, 16); sq += __shfl_xor(sq, 32);
;                 if (fq == 0) ssq[row * 16 + u.pn * 4 + wc] = sq; }
; __device__ __forceinline__ void phaseE(const Params& p, int layer, LAS unsigned char* lds, int bid, int nb) {
;     ...
;         unsigned* ctr = (unsigned*)(p.ws + ws::CTL) + CW_CTXC + (layer * 8 + (bid >> 3)) * 64;
;         asm volatile("s_waitcnt vmcnt(0)" ::: "memory");
;         __syncthreads();
;         if (tid == 0) {
;             __builtin_amdgcn_fence(__ATOMIC_RELEASE, "agent"); asm volatile("s_waitcnt vmcnt(0)" ::: "memory");
;             __hip_atomic_fetch_add(ctr, 1u, __ATOMIC_RELAXED, __HIP_MEMORY_SCOPE_AGENT);
.LBB0_1279:
	s_or_b64 exec, exec, s[0:1]
	v_readlane_b32 s0, v253, 61
	v_pk_add_f32 v[18:19], v[18:19], v[34:35]
	v_pk_add_f32 v[16:17], v[16:17], v[32:33]
	v_add_u32_e32 v20, s0, v1
	s_waitcnt lgkmcnt(0)
	v_ashrrev_i32_e32 v21, 31, v20
	v_readlane_b32 s0, v250, 6
	v_lshlrev_b64 v[22:23], 11, v[20:21]
	v_readlane_b32 s1, v250, 7
	v_pk_add_f32 v[14:15], v[14:15], v[30:31]
	v_pk_add_f32 v[12:13], v[12:13], v[28:29]
	v_lshl_add_u64 v[22:23], s[0:1], 0, v[22:23]
	v_lshl_add_u64 v[26:27], v[22:23], 0, v[2:3]
	global_load_dwordx4 v[22:25], v[26:27], off
	v_pk_mul_f32 v[18:19], v[46:47], v[18:19]
	v_pk_mul_f32 v[16:17], v[44:45], v[16:17]
	v_pk_mul_f32 v[14:15], v[54:55], v[14:15]
	v_pk_mul_f32 v[12:13], v[52:53], v[12:13]
	v_pk_add_f32 v[10:11], v[10:11], v[42:43]
	v_pk_add_f32 v[8:9], v[8:9], v[40:41]
	v_pk_add_f32 v[4:5], v[4:5], v[36:37]
	v_pk_mul_f32 v[10:11], v[50:51], v[10:11]
	v_pk_mul_f32 v[8:9], v[48:49], v[8:9]
	v_pk_add_f32 v[6:7], v[6:7], v[38:39]
	v_pk_mul_f32 v[4:5], v[64:65], v[4:5]
	v_pk_mul_f32 v[6:7], v[66:67], v[6:7]
	s_waitcnt vmcnt(0)
	v_lshlrev_b32_e32 v1, 16, v22
	v_and_b32_e32 v2, 0xffff0000, v22
	v_lshlrev_b32_e32 v22, 16, v23
	v_and_b32_e32 v23, 0xffff0000, v23
	v_lshlrev_b32_e32 v28, 16, v24
	v_and_b32_e32 v24, 0xffff0000, v24
	v_lshlrev_b32_e32 v29, 16, v25
	v_and_b32_e32 v25, 0xffff0000, v25
	v_add_f32_e32 v1, v16, v1
	v_add_f32_e32 v2, v17, v2
	v_add_f32_e32 v16, v18, v22
	v_add_f32_e32 v17, v19, v23
	v_add_f32_e32 v18, v12, v28
	v_add_f32_e32 v19, v13, v24
	v_add_f32_e32 v15, v15, v25
	v_add_f32_e32 v22, v14, v29
	v_cvt_pk_bf16_f32 v12, v1, v2
	v_cvt_pk_bf16_f32 v13, v16, v17
	v_cvt_pk_bf16_f32 v14, v18, v19
	v_cvt_pk_bf16_f32 v15, v22, v15
	global_load_dwordx4 v[16:19], v[26:27], off offset:256
	v_lshlrev_b32_e32 v1, 16, v12
	global_store_dwordx4 v[26:27], v[12:15], off sc1
	v_and_b32_e32 v2, 0xffff0000, v12
	v_lshlrev_b32_e32 v22, 16, v14
	v_lshlrev_b32_e32 v12, 16, v13
	v_and_b32_e32 v13, 0xffff0000, v13
	v_and_b32_e32 v14, 0xffff0000, v14
	v_mul_f32_e32 v2, v2, v2
	v_mul_f32_e32 v13, v13, v13
	v_lshlrev_b32_e32 v23, 16, v15
	v_and_b32_e32 v15, 0xffff0000, v15
	v_mul_f32_e32 v14, v14, v14
	v_fmac_f32_e32 v2, v1, v1
	v_fmac_f32_e32 v13, v12, v12
	v_mul_f32_e32 v15, v15, v15
	v_fmac_f32_e32 v14, v22, v22
	v_add_f32_e32 v1, v2, v13
	v_fmac_f32_e32 v15, v23, v23
	v_add_f32_e32 v1, v1, v14
	v_add_f32_e32 v1, v1, v15
	s_waitcnt vmcnt(1)
	v_lshlrev_b32_e32 v2, 16, v16
	v_and_b32_e32 v12, 0xffff0000, v16
	v_lshlrev_b32_e32 v13, 16, v17
	v_and_b32_e32 v14, 0xffff0000, v17
	v_lshlrev_b32_e32 v15, 16, v18
	v_and_b32_e32 v16, 0xffff0000, v18
	v_add_f32_e32 v2, v8, v2
	v_add_f32_e32 v8, v9, v12
	v_add_f32_e32 v9, v10, v13
	v_add_f32_e32 v10, v11, v14
	v_lshlrev_b32_e32 v17, 16, v19
	v_and_b32_e32 v18, 0xffff0000, v19
	v_add_f32_e32 v11, v4, v15
	v_add_f32_e32 v12, v5, v16
	v_cvt_pk_bf16_f32 v4, v2, v8
	v_cvt_pk_bf16_f32 v5, v9, v10
	v_add_f32_e32 v13, v6, v17
	v_and_b32_e32 v8, 0xffff0000, v4
	v_and_b32_e32 v10, 0xffff0000, v5
	v_add_f32_e32 v7, v7, v18
	v_cvt_pk_bf16_f32 v6, v11, v12
	v_lshlrev_b32_e32 v2, 16, v4
	v_lshlrev_b32_e32 v9, 16, v5
	v_and_b32_e32 v12, 0xffff0000, v6
	v_mul_f32_e32 v8, v8, v8
	v_mul_f32_e32 v10, v10, v10
	v_cvt_pk_bf16_f32 v7, v13, v7
	v_lshlrev_b32_e32 v11, 16, v6
	v_and_b32_e32 v14, 0xffff0000, v7
	v_mul_f32_e32 v12, v12, v12
	v_fmac_f32_e32 v8, v2, v2
	v_fmac_f32_e32 v10, v9, v9
	v_lshlrev_b32_e32 v13, 16, v7
	v_mul_f32_e32 v14, v14, v14
	v_fmac_f32_e32 v12, v11, v11
	v_add_f32_e32 v2, v8, v10
	v_add_f32_e32 v2, v2, v12
	v_fmac_f32_e32 v14, v13, v13
	v_add_f32_e32 v2, v2, v14
	v_add_f32_e32 v1, v1, v2
	ds_bpermute_b32 v2, v88, v1
	global_store_dwordx4 v[26:27], v[4:7], off offset:256 sc1
	s_waitcnt lgkmcnt(0)
	v_add_f32_e32 v1, v1, v2
	ds_bpermute_b32 v2, v89, v1
	s_and_saveexec_b64 s[0:1], vcc
	s_cbranch_execz .LBB0_1281
	v_readlane_b32 s4, v253, 56
	v_lshlrev_b64 v[4:5], 6, v[20:21]
	v_readlane_b32 s5, v253, 57
	s_lshl_b32 s30, s12, 2
	s_waitcnt lgkmcnt(0)
	v_add_f32_e32 v1, v1, v2
	v_lshl_add_u64 v[4:5], s[4:5], 0, v[4:5]
	v_lshl_add_u64 v[4:5], v[4:5], 0, s[30:31]
	global_store_dword v[4:5], v1, off sc1
.LBB0_1281:
	s_or_b64 exec, exec, s[0:1]
	s_waitcnt vmcnt(0)
	s_barrier
	s_waitcnt vmcnt(0)
	v_cmp_eq_u32_e32 vcc, 0, v96
	s_waitcnt lgkmcnt(0)
	s_barrier
	s_and_saveexec_b64 s[0:1], vcc
	s_cbranch_execz .LBB0_1284
	s_mov_b64 s[4:5], exec
	v_mbcnt_lo_u32_b32 v1, s4, 0
	s_waitcnt vmcnt(0)
	v_mbcnt_hi_u32_b32 v1, s5, v1
	v_cmp_eq_u32_e32 vcc, 0, v1
	s_and_b64 s[12:13], exec, vcc
	s_mov_b64 exec, s[12:13]
	s_cbranch_execz .LBB0_1284
	v_readlane_b32 s12, v255, 8
	v_readlane_b32 s13, v255, 9
	s_lshl_b32 s12, s12, 9
	v_readlane_b32 s13, v251, 0
	s_add_i32 s12, s12, s13
	s_ashr_i32 s13, s12, 31
	s_lshl_b64 s[12:13], s[12:13], 2
	v_readlane_b32 s16, v253, 62
	s_add_u32 s12, s16, s12
	v_readlane_b32 s16, v253, 63
	s_addc_u32 s13, s16, s13
	s_bcnt1_i32_b64 s4, s[4:5]
	v_mov_b32_e32 v1, s4
	global_atomic_add v3, v1, s[12:13]
